# on top of the P6 restructure: removed the 100 s_nop 0 pads between back-to-back same-accumulator bf16 MFMA pairs in the in-proj and out-proj K-loops
# baseline (speedup 1.0000x reference)
; #define PG8_STAGE_A(bufoff, soff, voff) do { _Pragma("unroll") for (int _i = 0; _i < 2; ++_i) \
;         __builtin_amdgcn_raw_ptr_buffer_load_lds(rsA, (LAS void*)(lds + (bufoff) + ldsw + _i * 8192), 16, (voff)[_i], (soff), 0, 0); } while (0)
; #define PG8_STAGE_B(bufoff, soff) do { _Pragma("unroll") for (int _i = 0; _i < 2; ++_i) \
;         __builtin_amdgcn_raw_ptr_buffer_load_lds(rsB, (LAS void*)(lds + (bufoff) + ldsw + _i * 8192), 16, voffB[_i], (soff), 0, 0); } while (0)
; #define PG8_LDA(dst, b, h) do { _Pragma("unroll") for (int m = 0; m < 4; ++m) dst[m] = PG8_LD8(lds + PG8_SA(b, h) + aoff + m * 2048); } while (0)
; #define PG8_LDB(dst, b, h) do { _Pragma("unroll") for (int n = 0; n < 2; ++n) dst[n] = PG8_LD8(lds + PG8_SB(b, h) + boff + n * 2048); } while (0)
; #define PG8_WAIT_V(n) asm volatile("s_waitcnt vmcnt(" #n ")" ::: "memory")
; #define PG8_WAIT_L(n) asm volatile("s_waitcnt lgkmcnt(" #n ")" ::: "memory")
; #define PG8_BAR __builtin_amdgcn_s_barrier()
; #define PG8_SCHED __builtin_amdgcn_sched_barrier(0)
; template <class Epi, class Sched, bool GATHER, bool ALIGN_EPI, bool SP2, bool FP8>
; __device__ __forceinline__ void gemm_phase(LAS unsigned char* lds, const Gemm g, const Sched& S, const Epi& E) {
;     ...
;             PG8_LDB(B0, 0, 0); PG8_LDB(B1, 0, 1); PG8_SCHED; PG8_LDA(At, 0, 0); PG8_STAGE_A(PG8_SA(1, 1), a1, vA1);
;             PG8_WAIT_V(8); PG8_WAIT_L(0); PG8_BAR; PG8_MMA(0, 0, At, B0); PG8_MMA(0, 1, At, B1); PG8_BAR; PG8_SCHED;
;             PG8_LDA(At, 0, 1); PG8_STAGE_B(PG8_SB(0, 0), b2); PG8_STAGE_B(PG8_SB(0, 1), b2 + hstep); PG8_STAGE_A(PG8_SA(0, 0), a2, va20);
.LBB0_191:
	v_add_u32_e32 v130, 0x10000, v186
	v_add_u32_e32 v131, 0x14000, v186
	ds_read_b128 v[158:161], v130
	ds_read_b128 v[154:157], v130 offset:1024
	ds_read_b128 v[150:153], v130 offset:2048
	ds_read_b128 v[146:149], v130 offset:3072
	ds_read_b128 v[142:145], v131
	ds_read_b128 v[138:141], v131 offset:1024
	ds_read_b128 v[134:137], v131 offset:2048
	ds_read_b128 v[130:133], v131 offset:3072
	s_add_i32 s53, s50, 0x80
	s_and_b64 s[56:57], s[10:11], exec
	s_cselect_b32 s57, s48, s53
	s_or_b32 s53, s57, 0x80
	s_and_b64 s[10:11], s[10:11], exec
	s_cselect_b32 s56, s49, s51
	s_mov_b32 m0, s39
	ds_read_b128 v[188:191], v187
	ds_read_b128 v[192:195], v187 offset:1024
	ds_read_b128 v[196:199], v187 offset:2048
	ds_read_b128 v[200:203], v187 offset:3072
	ds_read_b128 v[204:207], v187 offset:4096
	ds_read_b128 v[208:211], v187 offset:5120
	ds_read_b128 v[212:215], v187 offset:6144
	ds_read_b128 v[216:219], v187 offset:7168
	buffer_load_dwordx4 v183, s[4:7], s50 offen lds
	s_mov_b32 m0, s40
	s_nop 0
	buffer_load_dwordx4 v184, s[4:7], s50 offen lds
	s_waitcnt vmcnt(8)
	s_waitcnt lgkmcnt(0)
	s_barrier
	s_setprio 1
	s_waitcnt lgkmcnt(7)
	v_mfma_f32_16x16x32_bf16 v[126:129], v[158:161], v[188:191], v[126:129]
	s_waitcnt lgkmcnt(6)
	v_mfma_f32_16x16x32_bf16 v[126:129], v[154:157], v[192:195], v[126:129]
	v_mfma_f32_16x16x32_bf16 v[122:125], v[150:153], v[188:191], v[122:125]
	v_mfma_f32_16x16x32_bf16 v[122:125], v[146:149], v[192:195], v[122:125]
	s_waitcnt lgkmcnt(5)
	v_mfma_f32_16x16x32_bf16 v[118:121], v[158:161], v[196:199], v[118:121]
	s_waitcnt lgkmcnt(4)
	v_mfma_f32_16x16x32_bf16 v[118:121], v[154:157], v[200:203], v[118:121]
	v_mfma_f32_16x16x32_bf16 v[110:113], v[150:153], v[196:199], v[110:113]
	v_mfma_f32_16x16x32_bf16 v[110:113], v[146:149], v[200:203], v[110:113]
	s_waitcnt lgkmcnt(3)
	v_mfma_f32_16x16x32_bf16 v[102:105], v[158:161], v[204:207], v[102:105]
	s_waitcnt lgkmcnt(2)
	v_mfma_f32_16x16x32_bf16 v[102:105], v[154:157], v[208:211], v[102:105]
	v_mfma_f32_16x16x32_bf16 v[94:97], v[150:153], v[204:207], v[94:97]
	v_mfma_f32_16x16x32_bf16 v[94:97], v[146:149], v[208:211], v[94:97]
	s_waitcnt lgkmcnt(1)
	v_mfma_f32_16x16x32_bf16 v[86:89], v[158:161], v[212:215], v[86:89]
	s_waitcnt lgkmcnt(0)
	v_mfma_f32_16x16x32_bf16 v[86:89], v[154:157], v[216:219], v[86:89]
	v_mfma_f32_16x16x32_bf16 v[78:81], v[150:153], v[212:215], v[78:81]
	v_mfma_f32_16x16x32_bf16 v[78:81], v[146:149], v[216:219], v[78:81]
	s_setprio 0
	s_setprio 1
	v_mfma_f32_16x16x32_bf16 v[114:117], v[142:145], v[188:191], v[114:117]
	v_mfma_f32_16x16x32_bf16 v[114:117], v[138:141], v[192:195], v[114:117]
	v_mfma_f32_16x16x32_bf16 v[106:109], v[134:137], v[188:191], v[106:109]
	v_mfma_f32_16x16x32_bf16 v[106:109], v[130:133], v[192:195], v[106:109]
	v_mfma_f32_16x16x32_bf16 v[98:101], v[142:145], v[196:199], v[98:101]
	v_mfma_f32_16x16x32_bf16 v[98:101], v[138:141], v[200:203], v[98:101]
	v_mfma_f32_16x16x32_bf16 v[90:93], v[134:137], v[196:199], v[90:93]
	v_mfma_f32_16x16x32_bf16 v[90:93], v[130:133], v[200:203], v[90:93]
	v_mfma_f32_16x16x32_bf16 v[82:85], v[142:145], v[204:207], v[82:85]
	v_mfma_f32_16x16x32_bf16 v[82:85], v[138:141], v[208:211], v[82:85]
	v_mfma_f32_16x16x32_bf16 v[74:77], v[134:137], v[204:207], v[74:77]
	v_mfma_f32_16x16x32_bf16 v[74:77], v[130:133], v[208:211], v[74:77]
	v_mfma_f32_16x16x32_bf16 v[70:73], v[142:145], v[212:215], v[70:73]
	v_mfma_f32_16x16x32_bf16 v[70:73], v[138:141], v[216:219], v[70:73]
	v_mfma_f32_16x16x32_bf16 v[66:69], v[134:137], v[212:215], v[66:69]
	v_mfma_f32_16x16x32_bf16 v[66:69], v[130:133], v[216:219], v[66:69]
	s_setprio 0
	s_barrier
	s_mov_b32 m0, s23
	s_mov_b32 s10, s6
	s_mov_b32 s11, s7
	ds_read_b128 v[188:191], v187 offset:16384
	ds_read_b128 v[192:195], v187 offset:17408
	ds_read_b128 v[196:199], v187 offset:18432
	ds_read_b128 v[200:203], v187 offset:19456
	ds_read_b128 v[204:207], v187 offset:20480
	ds_read_b128 v[208:211], v187 offset:21504
	ds_read_b128 v[212:215], v187 offset:22528
	ds_read_b128 v[216:219], v187 offset:23552
	buffer_load_dwordx4 v165, s[8:11], s56 offen lds
	s_mov_b32 m0, s24
	s_add_i32 s58, s56, 0x80000
	buffer_load_dwordx4 v180, s[8:11], s56 offen lds
	s_mov_b32 m0, s25
	s_nop 0
	buffer_load_dwordx4 v165, s[8:11], s58 offen lds
	s_mov_b32 m0, s26
	s_nop 0
	buffer_load_dwordx4 v180, s[8:11], s58 offen lds
	s_mov_b32 m0, s22
	s_nop 0
	buffer_load_dwordx4 v181, s[4:7], s57 offen lds
	s_mov_b32 m0, s27
	s_nop 0
	buffer_load_dwordx4 v182, s[4:7], s57 offen lds
	s_waitcnt vmcnt(8)
	s_waitcnt lgkmcnt(0)
	s_barrier
; #define PG8_STAGE_A(bufoff, soff, voff) do { _Pragma("unroll") for (int _i = 0; _i < 2; ++_i) \
;         __builtin_amdgcn_raw_ptr_buffer_load_lds(rsA, (LAS void*)(lds + (bufoff) + ldsw + _i * 8192), 16, (voff)[_i], (soff), 0, 0); } while (0)
; #define PG8_STAGE_B(bufoff, soff) do { _Pragma("unroll") for (int _i = 0; _i < 2; ++_i) \
;         __builtin_amdgcn_raw_ptr_buffer_load_lds(rsB, (LAS void*)(lds + (bufoff) + ldsw + _i * 8192), 16, voffB[_i], (soff), 0, 0); } while (0)
; #define PG8_LDA(dst, b, h) do { _Pragma("unroll") for (int m = 0; m < 4; ++m) dst[m] = PG8_LD8(lds + PG8_SA(b, h) + aoff + m * 2048); } while (0)
; #define PG8_LDB(dst, b, h) do { _Pragma("unroll") for (int n = 0; n < 2; ++n) dst[n] = PG8_LD8(lds + PG8_SB(b, h) + boff + n * 2048); } while (0)
; #define PG8_WAIT_V(n) asm volatile("s_waitcnt vmcnt(" #n ")" ::: "memory")
; #define PG8_WAIT_L(n) asm volatile("s_waitcnt lgkmcnt(" #n ")" ::: "memory")
; #define PG8_BAR __builtin_amdgcn_s_barrier()
; #define PG8_SCHED __builtin_amdgcn_sched_barrier(0)
; template <class Epi, class Sched, bool GATHER, bool ALIGN_EPI, bool SP2, bool FP8>
; __device__ __forceinline__ void gemm_phase(LAS unsigned char* lds, const Gemm g, const Sched& S, const Epi& E) {
;     ...
;             PG8_LDA(At, 0, 1); PG8_STAGE_B(PG8_SB(0, 0), b2); PG8_STAGE_B(PG8_SB(0, 1), b2 + hstep); PG8_STAGE_A(PG8_SA(0, 0), a2, va20);
;             PG8_WAIT_V(8); PG8_WAIT_L(0); PG8_BAR; PG8_MMA(1, 0, At, B0); PG8_MMA(1, 1, At, B1); PG8_BAR; PG8_SCHED;
;             PG8_LDB(B0, 1, 0); PG8_LDB(B1, 1, 1); PG8_SCHED; PG8_LDA(At, 1, 0); PG8_STAGE_A(PG8_SA(0, 1), a2, va21);
;             PG8_WAIT_V(8); PG8_WAIT_L(0); PG8_BAR; PG8_MMA(0, 0, At, B0); PG8_MMA(0, 1, At, B1); PG8_BAR; PG8_SCHED;
	s_setprio 1
	s_waitcnt lgkmcnt(7)
	v_mfma_f32_16x16x32_bf16 v[62:65], v[158:161], v[188:191], v[62:65]
	s_waitcnt lgkmcnt(6)
	v_mfma_f32_16x16x32_bf16 v[62:65], v[154:157], v[192:195], v[62:65]
	v_mfma_f32_16x16x32_bf16 v[58:61], v[150:153], v[188:191], v[58:61]
	v_mfma_f32_16x16x32_bf16 v[58:61], v[146:149], v[192:195], v[58:61]
	s_waitcnt lgkmcnt(5)
	v_mfma_f32_16x16x32_bf16 v[54:57], v[158:161], v[196:199], v[54:57]
	s_waitcnt lgkmcnt(4)
	v_mfma_f32_16x16x32_bf16 v[54:57], v[154:157], v[200:203], v[54:57]
	v_mfma_f32_16x16x32_bf16 v[46:49], v[150:153], v[196:199], v[46:49]
	v_mfma_f32_16x16x32_bf16 v[46:49], v[146:149], v[200:203], v[46:49]
	s_waitcnt lgkmcnt(3)
	v_mfma_f32_16x16x32_bf16 v[38:41], v[158:161], v[204:207], v[38:41]
	s_waitcnt lgkmcnt(2)
	v_mfma_f32_16x16x32_bf16 v[38:41], v[154:157], v[208:211], v[38:41]
	v_mfma_f32_16x16x32_bf16 v[30:33], v[150:153], v[204:207], v[30:33]
	v_mfma_f32_16x16x32_bf16 v[30:33], v[146:149], v[208:211], v[30:33]
	s_waitcnt lgkmcnt(1)
	v_mfma_f32_16x16x32_bf16 v[22:25], v[158:161], v[212:215], v[22:25]
	s_waitcnt lgkmcnt(0)
	v_mfma_f32_16x16x32_bf16 v[22:25], v[154:157], v[216:219], v[22:25]
	v_mfma_f32_16x16x32_bf16 v[14:17], v[150:153], v[212:215], v[14:17]
	v_mfma_f32_16x16x32_bf16 v[14:17], v[146:149], v[216:219], v[14:17]
	s_setprio 0
	s_setprio 1
	v_mfma_f32_16x16x32_bf16 v[50:53], v[142:145], v[188:191], v[50:53]
	v_mfma_f32_16x16x32_bf16 v[50:53], v[138:141], v[192:195], v[50:53]
	v_mfma_f32_16x16x32_bf16 v[42:45], v[134:137], v[188:191], v[42:45]
	v_mfma_f32_16x16x32_bf16 v[42:45], v[130:133], v[192:195], v[42:45]
	v_mfma_f32_16x16x32_bf16 v[34:37], v[142:145], v[196:199], v[34:37]
	v_mfma_f32_16x16x32_bf16 v[34:37], v[138:141], v[200:203], v[34:37]
	v_mfma_f32_16x16x32_bf16 v[26:29], v[134:137], v[196:199], v[26:29]
	v_mfma_f32_16x16x32_bf16 v[26:29], v[130:133], v[200:203], v[26:29]
	v_mfma_f32_16x16x32_bf16 v[18:21], v[142:145], v[204:207], v[18:21]
	v_mfma_f32_16x16x32_bf16 v[18:21], v[138:141], v[208:211], v[18:21]
	v_mfma_f32_16x16x32_bf16 v[10:13], v[134:137], v[204:207], v[10:13]
	v_mfma_f32_16x16x32_bf16 v[10:13], v[130:133], v[208:211], v[10:13]
	v_mfma_f32_16x16x32_bf16 v[6:9], v[142:145], v[212:215], v[6:9]
	v_mfma_f32_16x16x32_bf16 v[6:9], v[138:141], v[216:219], v[6:9]
	v_mfma_f32_16x16x32_bf16 v[2:5], v[134:137], v[212:215], v[2:5]
	v_mfma_f32_16x16x32_bf16 v[2:5], v[130:133], v[216:219], v[2:5]
	s_setprio 0
	s_barrier
	v_add_u32_e32 v142, 0x18000, v186
	v_add_u32_e32 v158, 0x1c000, v186
	ds_read_b128 v[130:133], v142
	ds_read_b128 v[134:137], v142 offset:1024
	ds_read_b128 v[138:141], v142 offset:2048
	ds_read_b128 v[142:145], v142 offset:3072
	ds_read_b128 v[146:149], v158
	ds_read_b128 v[150:153], v158 offset:1024
	ds_read_b128 v[154:157], v158 offset:2048
	ds_read_b128 v[158:161], v158 offset:3072
	s_mov_b32 m0, s28
	ds_read_b128 v[188:191], v187 offset:32768
	ds_read_b128 v[192:195], v187 offset:33792
	ds_read_b128 v[196:199], v187 offset:34816
	ds_read_b128 v[200:203], v187 offset:35840
	ds_read_b128 v[204:207], v187 offset:36864
	ds_read_b128 v[208:211], v187 offset:37888
	ds_read_b128 v[212:215], v187 offset:38912
	ds_read_b128 v[216:219], v187 offset:39936
	buffer_load_dwordx4 v183, s[4:7], s57 offen lds
	s_mov_b32 m0, s29
	s_nop 0
	buffer_load_dwordx4 v184, s[4:7], s57 offen lds
	s_waitcnt vmcnt(8)
	s_waitcnt lgkmcnt(0)
	s_barrier
	s_setprio 1
	s_waitcnt lgkmcnt(7)
	v_mfma_f32_16x16x32_bf16 v[126:129], v[130:133], v[188:191], v[126:129]
	s_waitcnt lgkmcnt(6)
	v_mfma_f32_16x16x32_bf16 v[126:129], v[134:137], v[192:195], v[126:129]
	v_mfma_f32_16x16x32_bf16 v[122:125], v[138:141], v[188:191], v[122:125]
	v_mfma_f32_16x16x32_bf16 v[122:125], v[142:145], v[192:195], v[122:125]
	s_waitcnt lgkmcnt(5)
	v_mfma_f32_16x16x32_bf16 v[118:121], v[130:133], v[196:199], v[118:121]
	s_waitcnt lgkmcnt(4)
	v_mfma_f32_16x16x32_bf16 v[118:121], v[134:137], v[200:203], v[118:121]
	v_mfma_f32_16x16x32_bf16 v[110:113], v[138:141], v[196:199], v[110:113]
	v_mfma_f32_16x16x32_bf16 v[110:113], v[142:145], v[200:203], v[110:113]
	s_waitcnt lgkmcnt(3)
	v_mfma_f32_16x16x32_bf16 v[102:105], v[130:133], v[204:207], v[102:105]
	s_waitcnt lgkmcnt(2)
	v_mfma_f32_16x16x32_bf16 v[102:105], v[134:137], v[208:211], v[102:105]
	v_mfma_f32_16x16x32_bf16 v[94:97], v[138:141], v[204:207], v[94:97]
	v_mfma_f32_16x16x32_bf16 v[94:97], v[142:145], v[208:211], v[94:97]
	s_waitcnt lgkmcnt(1)
	v_mfma_f32_16x16x32_bf16 v[86:89], v[130:133], v[212:215], v[86:89]
	s_waitcnt lgkmcnt(0)
	v_mfma_f32_16x16x32_bf16 v[86:89], v[134:137], v[216:219], v[86:89]
	v_mfma_f32_16x16x32_bf16 v[78:81], v[138:141], v[212:215], v[78:81]
	v_mfma_f32_16x16x32_bf16 v[78:81], v[142:145], v[216:219], v[78:81]
	s_setprio 0
	s_setprio 1
	v_mfma_f32_16x16x32_bf16 v[114:117], v[146:149], v[188:191], v[114:117]
	v_mfma_f32_16x16x32_bf16 v[114:117], v[150:153], v[192:195], v[114:117]
	v_mfma_f32_16x16x32_bf16 v[106:109], v[154:157], v[188:191], v[106:109]
	v_mfma_f32_16x16x32_bf16 v[106:109], v[158:161], v[192:195], v[106:109]
	v_mfma_f32_16x16x32_bf16 v[98:101], v[146:149], v[196:199], v[98:101]
	v_mfma_f32_16x16x32_bf16 v[98:101], v[150:153], v[200:203], v[98:101]
	v_mfma_f32_16x16x32_bf16 v[90:93], v[154:157], v[196:199], v[90:93]
	v_mfma_f32_16x16x32_bf16 v[90:93], v[158:161], v[200:203], v[90:93]
	v_mfma_f32_16x16x32_bf16 v[82:85], v[146:149], v[204:207], v[82:85]
	v_mfma_f32_16x16x32_bf16 v[82:85], v[150:153], v[208:211], v[82:85]
	v_mfma_f32_16x16x32_bf16 v[74:77], v[154:157], v[204:207], v[74:77]
	v_mfma_f32_16x16x32_bf16 v[74:77], v[158:161], v[208:211], v[74:77]
	v_mfma_f32_16x16x32_bf16 v[70:73], v[146:149], v[212:215], v[70:73]
	v_mfma_f32_16x16x32_bf16 v[70:73], v[150:153], v[216:219], v[70:73]
	v_mfma_f32_16x16x32_bf16 v[66:69], v[154:157], v[212:215], v[66:69]
	v_mfma_f32_16x16x32_bf16 v[66:69], v[158:161], v[216:219], v[66:69]
	s_setprio 0
	s_barrier
; #define PG8_STAGE_A(bufoff, soff, voff) do { _Pragma("unroll") for (int _i = 0; _i < 2; ++_i) \
;         __builtin_amdgcn_raw_ptr_buffer_load_lds(rsA, (LAS void*)(lds + (bufoff) + ldsw + _i * 8192), 16, (voff)[_i], (soff), 0, 0); } while (0)
; #define PG8_STAGE_B(bufoff, soff) do { _Pragma("unroll") for (int _i = 0; _i < 2; ++_i) \
;         __builtin_amdgcn_raw_ptr_buffer_load_lds(rsB, (LAS void*)(lds + (bufoff) + ldsw + _i * 8192), 16, voffB[_i], (soff), 0, 0); } while (0)
; #define PG8_LDA(dst, b, h) do { _Pragma("unroll") for (int m = 0; m < 4; ++m) dst[m] = PG8_LD8(lds + PG8_SA(b, h) + aoff + m * 2048); } while (0)
; #define PG8_LDB(dst, b, h) do { _Pragma("unroll") for (int n = 0; n < 2; ++n) dst[n] = PG8_LD8(lds + PG8_SB(b, h) + boff + n * 2048); } while (0)
; #define PG8_WAIT_V(n) asm volatile("s_waitcnt vmcnt(" #n ")" ::: "memory")
; #define PG8_WAIT_L(n) asm volatile("s_waitcnt lgkmcnt(" #n ")" ::: "memory")
; #define PG8_BAR __builtin_amdgcn_s_barrier()
; #define PG8_SCHED __builtin_amdgcn_sched_barrier(0)
; template <class Epi, class Sched, bool GATHER, bool ALIGN_EPI, bool SP2, bool FP8>
; __device__ __forceinline__ void gemm_phase(LAS unsigned char* lds, const Gemm g, const Sched& S, const Epi& E) {
;     ...
;         for (int t = 0; t < nt; t += 2) {
;     ...
;             PG8_LDB(B0, 1, 0); PG8_LDB(B1, 1, 1); PG8_SCHED; PG8_LDA(At, 1, 0); PG8_STAGE_A(PG8_SA(0, 1), a2, va21);
;             PG8_WAIT_V(8); PG8_WAIT_L(0); PG8_BAR; PG8_MMA(0, 0, At, B0); PG8_MMA(0, 1, At, B1); PG8_BAR; PG8_SCHED;
;             PG8_LDA(At, 1, 1); PG8_STAGE_B(PG8_SB(1, 0), b3); PG8_STAGE_B(PG8_SB(1, 1), b3 + hstep); PG8_STAGE_A(PG8_SA(1, 0), a3, va20);
;             PG8_WAIT_V(8); PG8_WAIT_L(0); PG8_BAR; PG8_MMA(1, 0, At, B0); PG8_MMA(1, 1, At, B1); PG8_BAR; PG8_SCHED;
	s_mov_b32 m0, s31
	s_or_b32 s57, s56, 0x80
	ds_read_b128 v[188:191], v187 offset:49152
	ds_read_b128 v[192:195], v187 offset:50176
	ds_read_b128 v[196:199], v187 offset:51200
	ds_read_b128 v[200:203], v187 offset:52224
	ds_read_b128 v[204:207], v187 offset:53248
	ds_read_b128 v[208:211], v187 offset:54272
	ds_read_b128 v[212:215], v187 offset:55296
	ds_read_b128 v[216:219], v187 offset:56320
	buffer_load_dwordx4 v165, s[8:11], s57 offen lds
	s_mov_b32 m0, s34
	s_add_i32 s56, s56, 0x80080
	buffer_load_dwordx4 v180, s[8:11], s57 offen lds
	s_mov_b32 m0, s37
	s_nop 0
	buffer_load_dwordx4 v165, s[8:11], s56 offen lds
	s_mov_b32 m0, s38
	s_nop 0
	buffer_load_dwordx4 v180, s[8:11], s56 offen lds
	s_mov_b32 m0, s35
	s_nop 0
	buffer_load_dwordx4 v181, s[4:7], s53 offen lds
	s_mov_b32 m0, s36
	s_nop 0
	buffer_load_dwordx4 v182, s[4:7], s53 offen lds
	s_waitcnt vmcnt(8)
	s_waitcnt lgkmcnt(0)
	s_barrier
	s_setprio 1
	s_waitcnt lgkmcnt(7)
	v_mfma_f32_16x16x32_bf16 v[62:65], v[130:133], v[188:191], v[62:65]
	s_waitcnt lgkmcnt(6)
	v_mfma_f32_16x16x32_bf16 v[62:65], v[134:137], v[192:195], v[62:65]
	v_mfma_f32_16x16x32_bf16 v[58:61], v[138:141], v[188:191], v[58:61]
	v_mfma_f32_16x16x32_bf16 v[58:61], v[142:145], v[192:195], v[58:61]
	s_waitcnt lgkmcnt(5)
	v_mfma_f32_16x16x32_bf16 v[54:57], v[130:133], v[196:199], v[54:57]
	s_waitcnt lgkmcnt(4)
	v_mfma_f32_16x16x32_bf16 v[54:57], v[134:137], v[200:203], v[54:57]
	v_mfma_f32_16x16x32_bf16 v[46:49], v[138:141], v[196:199], v[46:49]
	v_mfma_f32_16x16x32_bf16 v[46:49], v[142:145], v[200:203], v[46:49]
	s_waitcnt lgkmcnt(3)
	v_mfma_f32_16x16x32_bf16 v[38:41], v[130:133], v[204:207], v[38:41]
	s_waitcnt lgkmcnt(2)
	v_mfma_f32_16x16x32_bf16 v[38:41], v[134:137], v[208:211], v[38:41]
	v_mfma_f32_16x16x32_bf16 v[30:33], v[138:141], v[204:207], v[30:33]
	v_mfma_f32_16x16x32_bf16 v[30:33], v[142:145], v[208:211], v[30:33]
	s_waitcnt lgkmcnt(1)
	v_mfma_f32_16x16x32_bf16 v[22:25], v[130:133], v[212:215], v[22:25]
	s_waitcnt lgkmcnt(0)
	v_mfma_f32_16x16x32_bf16 v[22:25], v[134:137], v[216:219], v[22:25]
	v_mfma_f32_16x16x32_bf16 v[14:17], v[138:141], v[212:215], v[14:17]
	v_mfma_f32_16x16x32_bf16 v[14:17], v[142:145], v[216:219], v[14:17]
	s_setprio 0
	s_setprio 1
	v_mfma_f32_16x16x32_bf16 v[50:53], v[146:149], v[188:191], v[50:53]
	v_mfma_f32_16x16x32_bf16 v[50:53], v[150:153], v[192:195], v[50:53]
	v_mfma_f32_16x16x32_bf16 v[42:45], v[154:157], v[188:191], v[42:45]
	v_mfma_f32_16x16x32_bf16 v[42:45], v[158:161], v[192:195], v[42:45]
	v_mfma_f32_16x16x32_bf16 v[34:37], v[146:149], v[196:199], v[34:37]
	v_mfma_f32_16x16x32_bf16 v[34:37], v[150:153], v[200:203], v[34:37]
	v_mfma_f32_16x16x32_bf16 v[26:29], v[154:157], v[196:199], v[26:29]
	v_mfma_f32_16x16x32_bf16 v[26:29], v[158:161], v[200:203], v[26:29]
	v_mfma_f32_16x16x32_bf16 v[18:21], v[146:149], v[204:207], v[18:21]
	v_mfma_f32_16x16x32_bf16 v[18:21], v[150:153], v[208:211], v[18:21]
	v_mfma_f32_16x16x32_bf16 v[10:13], v[154:157], v[204:207], v[10:13]
	v_mfma_f32_16x16x32_bf16 v[10:13], v[158:161], v[208:211], v[10:13]
	v_mfma_f32_16x16x32_bf16 v[6:9], v[146:149], v[212:215], v[6:9]
	v_mfma_f32_16x16x32_bf16 v[6:9], v[150:153], v[216:219], v[6:9]
	v_mfma_f32_16x16x32_bf16 v[2:5], v[154:157], v[212:215], v[2:5]
	v_mfma_f32_16x16x32_bf16 v[2:5], v[158:161], v[216:219], v[2:5]
	s_setprio 0
	s_barrier
	s_add_i32 s52, s52, 2
	s_addk_i32 s50, 0x100
	s_addk_i32 s51, 0x100
	s_cmp_gt_u32 s52, 29
	s_cbranch_scc1 .LBB0_187

; #define PG8_STAGE_A(bufoff, soff, voff) do { _Pragma("unroll") for (int _i = 0; _i < 2; ++_i) \
;         __builtin_amdgcn_raw_ptr_buffer_load_lds(rsA, (LAS void*)(lds + (bufoff) + ldsw + _i * 8192), 16, (voff)[_i], (soff), 0, 0); } while (0)
; #define PG8_STAGE_B(bufoff, soff) do { _Pragma("unroll") for (int _i = 0; _i < 2; ++_i) \
;         __builtin_amdgcn_raw_ptr_buffer_load_lds(rsB, (LAS void*)(lds + (bufoff) + ldsw + _i * 8192), 16, voffB[_i], (soff), 0, 0); } while (0)
; #define PG8_LDA(dst, b, h) do { _Pragma("unroll") for (int m = 0; m < 4; ++m) dst[m] = PG8_LD8(lds + PG8_SA(b, h) + aoff + m * 2048); } while (0)
; #define PG8_LDB(dst, b, h) do { _Pragma("unroll") for (int n = 0; n < 2; ++n) dst[n] = PG8_LD8(lds + PG8_SB(b, h) + boff + n * 2048); } while (0)
; #define PG8_WAIT_V(n) asm volatile("s_waitcnt vmcnt(" #n ")" ::: "memory")
; #define PG8_WAIT_L(n) asm volatile("s_waitcnt lgkmcnt(" #n ")" ::: "memory")
; #define PG8_BAR __builtin_amdgcn_s_barrier()
; #define PG8_SCHED __builtin_amdgcn_sched_barrier(0)
; template <class Epi, class Sched, bool GATHER, bool ALIGN_EPI, bool SP2, bool FP8>
; __device__ __forceinline__ void gemm_phase(LAS unsigned char* lds, const Gemm g, const Sched& S, const Epi& E) {
;     ...
;             PG8_LDB(B0, 0, 0); PG8_LDB(B1, 0, 1); PG8_SCHED; PG8_LDA(At, 0, 0); PG8_STAGE_A(PG8_SA(1, 1), a1, vA1);
;             PG8_WAIT_V(8); PG8_WAIT_L(0); PG8_BAR; PG8_MMA(0, 0, At, B0); PG8_MMA(0, 1, At, B1); PG8_BAR; PG8_SCHED;
;             PG8_LDA(At, 0, 1); PG8_STAGE_B(PG8_SB(0, 0), b2); PG8_STAGE_B(PG8_SB(0, 1), b2 + hstep); PG8_STAGE_A(PG8_SA(0, 0), a2, va20);
;             PG8_WAIT_V(8); PG8_WAIT_L(0); PG8_BAR; PG8_MMA(1, 0, At, B0); PG8_MMA(1, 1, At, B1); PG8_BAR; PG8_SCHED;
.LBB0_708:
	ds_read_b128 v[158:161], v172
	ds_read_b128 v[154:157], v172 offset:1024
	ds_read_b128 v[150:153], v172 offset:2048
	ds_read_b128 v[146:149], v172 offset:3072
	ds_read_b128 v[142:145], v173
	ds_read_b128 v[138:141], v173 offset:1024
	ds_read_b128 v[134:137], v173 offset:2048
	ds_read_b128 v[130:133], v173 offset:3072
	s_add_i32 s10, s77, 0x80
	s_cmp_eq_u32 s79, 28
	s_cselect_b32 s82, s75, s10
	s_cselect_b32 s81, s76, s78
	s_or_b32 s80, s82, 0x80
	s_mov_b32 m0, s52
	ds_read_b128 v[178:181], v174
	ds_read_b128 v[182:185], v174 offset:1024
	ds_read_b128 v[186:189], v174 offset:2048
	ds_read_b128 v[190:193], v174 offset:3072
	ds_read_b128 v[194:197], v174 offset:4096
	ds_read_b128 v[198:201], v174 offset:5120
	ds_read_b128 v[202:205], v174 offset:6144
	ds_read_b128 v[206:209], v174 offset:7168
	buffer_load_dwordx4 v170, s[4:7], s77 offen lds
	s_mov_b32 m0, s53
	s_nop 0
	buffer_load_dwordx4 v171, s[4:7], s77 offen lds
	s_waitcnt vmcnt(8)
	s_waitcnt lgkmcnt(0)
	s_barrier
	s_setprio 1
	s_waitcnt lgkmcnt(0)
	v_mfma_f32_16x16x32_bf16 v[126:129], v[158:161], v[178:181], v[126:129]
	v_mfma_f32_16x16x32_bf16 v[126:129], v[154:157], v[182:185], v[126:129]
	v_mfma_f32_16x16x32_bf16 v[122:125], v[150:153], v[178:181], v[122:125]
	v_mfma_f32_16x16x32_bf16 v[122:125], v[146:149], v[182:185], v[122:125]
	v_mfma_f32_16x16x32_bf16 v[110:113], v[158:161], v[186:189], v[110:113]
	v_mfma_f32_16x16x32_bf16 v[110:113], v[154:157], v[190:193], v[110:113]
	v_mfma_f32_16x16x32_bf16 v[106:109], v[150:153], v[186:189], v[106:109]
	v_mfma_f32_16x16x32_bf16 v[106:109], v[146:149], v[190:193], v[106:109]
	v_mfma_f32_16x16x32_bf16 v[94:97], v[158:161], v[194:197], v[94:97]
	v_mfma_f32_16x16x32_bf16 v[94:97], v[154:157], v[198:201], v[94:97]
	v_mfma_f32_16x16x32_bf16 v[90:93], v[150:153], v[194:197], v[90:93]
	v_mfma_f32_16x16x32_bf16 v[90:93], v[146:149], v[198:201], v[90:93]
	v_mfma_f32_16x16x32_bf16 v[78:81], v[158:161], v[202:205], v[78:81]
	v_mfma_f32_16x16x32_bf16 v[78:81], v[154:157], v[206:209], v[78:81]
	v_mfma_f32_16x16x32_bf16 v[74:77], v[150:153], v[202:205], v[74:77]
	v_mfma_f32_16x16x32_bf16 v[74:77], v[146:149], v[206:209], v[74:77]
	s_setprio 0
	s_setprio 1
	v_mfma_f32_16x16x32_bf16 v[118:121], v[142:145], v[178:181], v[118:121]
	v_mfma_f32_16x16x32_bf16 v[118:121], v[138:141], v[182:185], v[118:121]
	v_mfma_f32_16x16x32_bf16 v[114:117], v[134:137], v[178:181], v[114:117]
	v_mfma_f32_16x16x32_bf16 v[114:117], v[130:133], v[182:185], v[114:117]
	v_mfma_f32_16x16x32_bf16 v[102:105], v[142:145], v[186:189], v[102:105]
	v_mfma_f32_16x16x32_bf16 v[102:105], v[138:141], v[190:193], v[102:105]
	v_mfma_f32_16x16x32_bf16 v[98:101], v[134:137], v[186:189], v[98:101]
	v_mfma_f32_16x16x32_bf16 v[98:101], v[130:133], v[190:193], v[98:101]
	v_mfma_f32_16x16x32_bf16 v[86:89], v[142:145], v[194:197], v[86:89]
	v_mfma_f32_16x16x32_bf16 v[86:89], v[138:141], v[198:201], v[86:89]
	v_mfma_f32_16x16x32_bf16 v[82:85], v[134:137], v[194:197], v[82:85]
	v_mfma_f32_16x16x32_bf16 v[82:85], v[130:133], v[198:201], v[82:85]
	v_mfma_f32_16x16x32_bf16 v[70:73], v[142:145], v[202:205], v[70:73]
	v_mfma_f32_16x16x32_bf16 v[70:73], v[138:141], v[206:209], v[70:73]
	v_mfma_f32_16x16x32_bf16 v[66:69], v[134:137], v[202:205], v[66:69]
	v_mfma_f32_16x16x32_bf16 v[66:69], v[130:133], v[206:209], v[66:69]
	s_setprio 0
	s_barrier
	s_mov_b32 m0, s37
	s_mov_b32 s10, s6
	s_mov_b32 s11, s7
	ds_read_b128 v[178:181], v174 offset:16384
	ds_read_b128 v[182:185], v174 offset:17408
	ds_read_b128 v[186:189], v174 offset:18432
	ds_read_b128 v[190:193], v174 offset:19456
	ds_read_b128 v[194:197], v174 offset:20480
	ds_read_b128 v[198:201], v174 offset:21504
	ds_read_b128 v[202:205], v174 offset:22528
	ds_read_b128 v[206:209], v174 offset:23552
	buffer_load_dwordx4 v1, s[8:11], s81 offen lds
	s_mov_b32 m0, s38
	s_add_i32 s83, s81, 0x80000
	buffer_load_dwordx4 v163, s[8:11], s81 offen lds
	s_mov_b32 m0, s39
	s_nop 0
	buffer_load_dwordx4 v1, s[8:11], s83 offen lds
	s_mov_b32 m0, s40
	s_nop 0
	buffer_load_dwordx4 v163, s[8:11], s83 offen lds
	s_mov_b32 m0, s36
	s_nop 0
	buffer_load_dwordx4 v168, s[4:7], s82 offen lds
	s_mov_b32 m0, s41
	s_nop 0
	buffer_load_dwordx4 v169, s[4:7], s82 offen lds
	s_waitcnt vmcnt(8)
	s_waitcnt lgkmcnt(0)
	s_barrier
	s_setprio 1
	s_waitcnt lgkmcnt(7)
	v_mfma_f32_16x16x32_bf16 v[62:65], v[158:161], v[178:181], v[62:65]
	s_waitcnt lgkmcnt(6)
	v_mfma_f32_16x16x32_bf16 v[62:65], v[154:157], v[182:185], v[62:65]
	v_mfma_f32_16x16x32_bf16 v[58:61], v[150:153], v[178:181], v[58:61]
	v_mfma_f32_16x16x32_bf16 v[58:61], v[146:149], v[182:185], v[58:61]
	s_waitcnt lgkmcnt(5)
	v_mfma_f32_16x16x32_bf16 v[46:49], v[158:161], v[186:189], v[46:49]
	s_waitcnt lgkmcnt(4)
	v_mfma_f32_16x16x32_bf16 v[46:49], v[154:157], v[190:193], v[46:49]
	v_mfma_f32_16x16x32_bf16 v[42:45], v[150:153], v[186:189], v[42:45]
	v_mfma_f32_16x16x32_bf16 v[42:45], v[146:149], v[190:193], v[42:45]
	s_waitcnt lgkmcnt(3)
	v_mfma_f32_16x16x32_bf16 v[30:33], v[158:161], v[194:197], v[30:33]
	s_waitcnt lgkmcnt(2)
	v_mfma_f32_16x16x32_bf16 v[30:33], v[154:157], v[198:201], v[30:33]
	v_mfma_f32_16x16x32_bf16 v[26:29], v[150:153], v[194:197], v[26:29]
	v_mfma_f32_16x16x32_bf16 v[26:29], v[146:149], v[198:201], v[26:29]
	s_waitcnt lgkmcnt(1)
	v_mfma_f32_16x16x32_bf16 v[14:17], v[158:161], v[202:205], v[14:17]
	s_waitcnt lgkmcnt(0)
	v_mfma_f32_16x16x32_bf16 v[14:17], v[154:157], v[206:209], v[14:17]
	v_mfma_f32_16x16x32_bf16 v[10:13], v[150:153], v[202:205], v[10:13]
	v_mfma_f32_16x16x32_bf16 v[10:13], v[146:149], v[206:209], v[10:13]
	s_setprio 0
	s_setprio 1
	v_mfma_f32_16x16x32_bf16 v[54:57], v[142:145], v[178:181], v[54:57]
	v_mfma_f32_16x16x32_bf16 v[54:57], v[138:141], v[182:185], v[54:57]
	v_mfma_f32_16x16x32_bf16 v[50:53], v[134:137], v[178:181], v[50:53]
	v_mfma_f32_16x16x32_bf16 v[50:53], v[130:133], v[182:185], v[50:53]
	v_mfma_f32_16x16x32_bf16 v[38:41], v[142:145], v[186:189], v[38:41]
	v_mfma_f32_16x16x32_bf16 v[38:41], v[138:141], v[190:193], v[38:41]
	v_mfma_f32_16x16x32_bf16 v[34:37], v[134:137], v[186:189], v[34:37]
	v_mfma_f32_16x16x32_bf16 v[34:37], v[130:133], v[190:193], v[34:37]
	v_mfma_f32_16x16x32_bf16 v[22:25], v[142:145], v[194:197], v[22:25]
	v_mfma_f32_16x16x32_bf16 v[22:25], v[138:141], v[198:201], v[22:25]
	v_mfma_f32_16x16x32_bf16 v[18:21], v[134:137], v[194:197], v[18:21]
	v_mfma_f32_16x16x32_bf16 v[18:21], v[130:133], v[198:201], v[18:21]
	v_mfma_f32_16x16x32_bf16 v[6:9], v[142:145], v[202:205], v[6:9]
	v_mfma_f32_16x16x32_bf16 v[6:9], v[138:141], v[206:209], v[6:9]
	v_mfma_f32_16x16x32_bf16 v[2:5], v[134:137], v[202:205], v[2:5]
	v_mfma_f32_16x16x32_bf16 v[2:5], v[130:133], v[206:209], v[2:5]
	s_setprio 0
	s_barrier
; #define PG8_STAGE_A(bufoff, soff, voff) do { _Pragma("unroll") for (int _i = 0; _i < 2; ++_i) \
;         __builtin_amdgcn_raw_ptr_buffer_load_lds(rsA, (LAS void*)(lds + (bufoff) + ldsw + _i * 8192), 16, (voff)[_i], (soff), 0, 0); } while (0)
; #define PG8_STAGE_B(bufoff, soff) do { _Pragma("unroll") for (int _i = 0; _i < 2; ++_i) \
;         __builtin_amdgcn_raw_ptr_buffer_load_lds(rsB, (LAS void*)(lds + (bufoff) + ldsw + _i * 8192), 16, voffB[_i], (soff), 0, 0); } while (0)
; #define PG8_LDA(dst, b, h) do { _Pragma("unroll") for (int m = 0; m < 4; ++m) dst[m] = PG8_LD8(lds + PG8_SA(b, h) + aoff + m * 2048); } while (0)
; #define PG8_LDB(dst, b, h) do { _Pragma("unroll") for (int n = 0; n < 2; ++n) dst[n] = PG8_LD8(lds + PG8_SB(b, h) + boff + n * 2048); } while (0)
; #define PG8_WAIT_V(n) asm volatile("s_waitcnt vmcnt(" #n ")" ::: "memory")
; #define PG8_WAIT_L(n) asm volatile("s_waitcnt lgkmcnt(" #n ")" ::: "memory")
; #define PG8_BAR __builtin_amdgcn_s_barrier()
; #define PG8_SCHED __builtin_amdgcn_sched_barrier(0)
; template <class Epi, class Sched, bool GATHER, bool ALIGN_EPI, bool SP2, bool FP8>
; __device__ __forceinline__ void gemm_phase(LAS unsigned char* lds, const Gemm g, const Sched& S, const Epi& E) {
;     ...
;             PG8_LDB(B0, 1, 0); PG8_LDB(B1, 1, 1); PG8_SCHED; PG8_LDA(At, 1, 0); PG8_STAGE_A(PG8_SA(0, 1), a2, va21);
;             PG8_WAIT_V(8); PG8_WAIT_L(0); PG8_BAR; PG8_MMA(0, 0, At, B0); PG8_MMA(0, 1, At, B1); PG8_BAR; PG8_SCHED;
;             PG8_LDA(At, 1, 1); PG8_STAGE_B(PG8_SB(1, 0), b3); PG8_STAGE_B(PG8_SB(1, 1), b3 + hstep); PG8_STAGE_A(PG8_SA(1, 0), a3, va20);
;             PG8_WAIT_V(8); PG8_WAIT_L(0); PG8_BAR; PG8_MMA(1, 0, At, B0); PG8_MMA(1, 1, At, B1); PG8_BAR; PG8_SCHED;
	ds_read_b128 v[130:133], v175
	ds_read_b128 v[134:137], v175 offset:1024
	ds_read_b128 v[138:141], v175 offset:2048
	ds_read_b128 v[142:145], v175 offset:3072
	ds_read_b128 v[146:149], v176
	ds_read_b128 v[150:153], v176 offset:1024
	ds_read_b128 v[154:157], v176 offset:2048
	ds_read_b128 v[158:161], v176 offset:3072
	s_mov_b32 m0, s42
	ds_read_b128 v[178:181], v174 offset:32768
	ds_read_b128 v[182:185], v174 offset:33792
	ds_read_b128 v[186:189], v174 offset:34816
	ds_read_b128 v[190:193], v174 offset:35840
	ds_read_b128 v[194:197], v174 offset:36864
	ds_read_b128 v[198:201], v174 offset:37888
	ds_read_b128 v[202:205], v174 offset:38912
	ds_read_b128 v[206:209], v174 offset:39936
	buffer_load_dwordx4 v170, s[4:7], s82 offen lds
	s_mov_b32 m0, s43
	s_nop 0
	buffer_load_dwordx4 v171, s[4:7], s82 offen lds
	s_waitcnt vmcnt(8)
	s_waitcnt lgkmcnt(0)
	s_barrier
	s_setprio 1
	s_waitcnt lgkmcnt(7)
	v_mfma_f32_16x16x32_bf16 v[126:129], v[130:133], v[178:181], v[126:129]
	s_waitcnt lgkmcnt(6)
	v_mfma_f32_16x16x32_bf16 v[126:129], v[134:137], v[182:185], v[126:129]
	v_mfma_f32_16x16x32_bf16 v[122:125], v[138:141], v[178:181], v[122:125]
	v_mfma_f32_16x16x32_bf16 v[122:125], v[142:145], v[182:185], v[122:125]
	s_waitcnt lgkmcnt(5)
	v_mfma_f32_16x16x32_bf16 v[110:113], v[130:133], v[186:189], v[110:113]
	s_waitcnt lgkmcnt(4)
	v_mfma_f32_16x16x32_bf16 v[110:113], v[134:137], v[190:193], v[110:113]
	v_mfma_f32_16x16x32_bf16 v[106:109], v[138:141], v[186:189], v[106:109]
	v_mfma_f32_16x16x32_bf16 v[106:109], v[142:145], v[190:193], v[106:109]
	s_waitcnt lgkmcnt(3)
	v_mfma_f32_16x16x32_bf16 v[94:97], v[130:133], v[194:197], v[94:97]
	s_waitcnt lgkmcnt(2)
	v_mfma_f32_16x16x32_bf16 v[94:97], v[134:137], v[198:201], v[94:97]
	v_mfma_f32_16x16x32_bf16 v[90:93], v[138:141], v[194:197], v[90:93]
	v_mfma_f32_16x16x32_bf16 v[90:93], v[142:145], v[198:201], v[90:93]
	s_waitcnt lgkmcnt(1)
	v_mfma_f32_16x16x32_bf16 v[78:81], v[130:133], v[202:205], v[78:81]
	s_waitcnt lgkmcnt(0)
	v_mfma_f32_16x16x32_bf16 v[78:81], v[134:137], v[206:209], v[78:81]
	v_mfma_f32_16x16x32_bf16 v[74:77], v[138:141], v[202:205], v[74:77]
	v_mfma_f32_16x16x32_bf16 v[74:77], v[142:145], v[206:209], v[74:77]
	s_setprio 0
	s_setprio 1
	v_mfma_f32_16x16x32_bf16 v[118:121], v[146:149], v[178:181], v[118:121]
	v_mfma_f32_16x16x32_bf16 v[118:121], v[150:153], v[182:185], v[118:121]
	v_mfma_f32_16x16x32_bf16 v[114:117], v[154:157], v[178:181], v[114:117]
	v_mfma_f32_16x16x32_bf16 v[114:117], v[158:161], v[182:185], v[114:117]
	v_mfma_f32_16x16x32_bf16 v[102:105], v[146:149], v[186:189], v[102:105]
	v_mfma_f32_16x16x32_bf16 v[102:105], v[150:153], v[190:193], v[102:105]
	v_mfma_f32_16x16x32_bf16 v[98:101], v[154:157], v[186:189], v[98:101]
	v_mfma_f32_16x16x32_bf16 v[98:101], v[158:161], v[190:193], v[98:101]
	v_mfma_f32_16x16x32_bf16 v[86:89], v[146:149], v[194:197], v[86:89]
	v_mfma_f32_16x16x32_bf16 v[86:89], v[150:153], v[198:201], v[86:89]
	v_mfma_f32_16x16x32_bf16 v[82:85], v[154:157], v[194:197], v[82:85]
	v_mfma_f32_16x16x32_bf16 v[82:85], v[158:161], v[198:201], v[82:85]
	v_mfma_f32_16x16x32_bf16 v[70:73], v[146:149], v[202:205], v[70:73]
	v_mfma_f32_16x16x32_bf16 v[70:73], v[150:153], v[206:209], v[70:73]
	v_mfma_f32_16x16x32_bf16 v[66:69], v[154:157], v[202:205], v[66:69]
	v_mfma_f32_16x16x32_bf16 v[66:69], v[158:161], v[206:209], v[66:69]
	s_setprio 0
	s_barrier
	s_mov_b32 m0, s46
	s_or_b32 s82, s81, 0x80
	ds_read_b128 v[178:181], v174 offset:49152
	ds_read_b128 v[182:185], v174 offset:50176
	ds_read_b128 v[186:189], v174 offset:51200
	ds_read_b128 v[190:193], v174 offset:52224
	ds_read_b128 v[194:197], v174 offset:53248
	ds_read_b128 v[198:201], v174 offset:54272
	ds_read_b128 v[202:205], v174 offset:55296
	ds_read_b128 v[206:209], v174 offset:56320
	buffer_load_dwordx4 v1, s[8:11], s82 offen lds
	s_mov_b32 m0, s47
	s_add_i32 s81, s81, 0x80080
	buffer_load_dwordx4 v163, s[8:11], s82 offen lds
	s_mov_b32 m0, s50
	s_nop 0
	buffer_load_dwordx4 v1, s[8:11], s81 offen lds
	s_mov_b32 m0, s51
	s_nop 0
	buffer_load_dwordx4 v163, s[8:11], s81 offen lds
	s_mov_b32 m0, s48
	s_nop 0
	buffer_load_dwordx4 v168, s[4:7], s80 offen lds
	s_mov_b32 m0, s49
	s_nop 0
	buffer_load_dwordx4 v169, s[4:7], s80 offen lds
	s_waitcnt vmcnt(8)
	s_waitcnt lgkmcnt(0)
	s_barrier
	s_setprio 1
	s_waitcnt lgkmcnt(7)
	v_mfma_f32_16x16x32_bf16 v[62:65], v[130:133], v[178:181], v[62:65]
	s_waitcnt lgkmcnt(6)
	v_mfma_f32_16x16x32_bf16 v[62:65], v[134:137], v[182:185], v[62:65]
	v_mfma_f32_16x16x32_bf16 v[58:61], v[138:141], v[178:181], v[58:61]
	v_mfma_f32_16x16x32_bf16 v[58:61], v[142:145], v[182:185], v[58:61]
	s_waitcnt lgkmcnt(5)
	v_mfma_f32_16x16x32_bf16 v[46:49], v[130:133], v[186:189], v[46:49]
	s_waitcnt lgkmcnt(4)
	v_mfma_f32_16x16x32_bf16 v[46:49], v[134:137], v[190:193], v[46:49]
	v_mfma_f32_16x16x32_bf16 v[42:45], v[138:141], v[186:189], v[42:45]
	v_mfma_f32_16x16x32_bf16 v[42:45], v[142:145], v[190:193], v[42:45]
	s_waitcnt lgkmcnt(3)
	v_mfma_f32_16x16x32_bf16 v[30:33], v[130:133], v[194:197], v[30:33]
	s_waitcnt lgkmcnt(2)
	v_mfma_f32_16x16x32_bf16 v[30:33], v[134:137], v[198:201], v[30:33]
	v_mfma_f32_16x16x32_bf16 v[26:29], v[138:141], v[194:197], v[26:29]
	v_mfma_f32_16x16x32_bf16 v[26:29], v[142:145], v[198:201], v[26:29]
	s_waitcnt lgkmcnt(1)
	v_mfma_f32_16x16x32_bf16 v[14:17], v[130:133], v[202:205], v[14:17]
	s_waitcnt lgkmcnt(0)
	v_mfma_f32_16x16x32_bf16 v[14:17], v[134:137], v[206:209], v[14:17]
	v_mfma_f32_16x16x32_bf16 v[10:13], v[138:141], v[202:205], v[10:13]
	v_mfma_f32_16x16x32_bf16 v[10:13], v[142:145], v[206:209], v[10:13]
	s_setprio 0
	s_setprio 1
	v_mfma_f32_16x16x32_bf16 v[54:57], v[146:149], v[178:181], v[54:57]
	v_mfma_f32_16x16x32_bf16 v[54:57], v[150:153], v[182:185], v[54:57]
	v_mfma_f32_16x16x32_bf16 v[50:53], v[154:157], v[178:181], v[50:53]
	v_mfma_f32_16x16x32_bf16 v[50:53], v[158:161], v[182:185], v[50:53]
	v_mfma_f32_16x16x32_bf16 v[38:41], v[146:149], v[186:189], v[38:41]
	v_mfma_f32_16x16x32_bf16 v[38:41], v[150:153], v[190:193], v[38:41]
	v_mfma_f32_16x16x32_bf16 v[34:37], v[154:157], v[186:189], v[34:37]
	v_mfma_f32_16x16x32_bf16 v[34:37], v[158:161], v[190:193], v[34:37]
	v_mfma_f32_16x16x32_bf16 v[22:25], v[146:149], v[194:197], v[22:25]
	v_mfma_f32_16x16x32_bf16 v[22:25], v[150:153], v[198:201], v[22:25]
	v_mfma_f32_16x16x32_bf16 v[18:21], v[154:157], v[194:197], v[18:21]
	v_mfma_f32_16x16x32_bf16 v[18:21], v[158:161], v[198:201], v[18:21]
	v_mfma_f32_16x16x32_bf16 v[6:9], v[146:149], v[202:205], v[6:9]
	v_mfma_f32_16x16x32_bf16 v[6:9], v[150:153], v[206:209], v[6:9]
	v_mfma_f32_16x16x32_bf16 v[2:5], v[154:157], v[202:205], v[2:5]
	v_mfma_f32_16x16x32_bf16 v[2:5], v[158:161], v[206:209], v[2:5]
	s_setprio 0
	s_barrier
; #define LAS __attribute__((address_space(3)))
; #define EPO_LOAD(dst, g) do { const size_t off_ = base + (size_t)(((g) >> 2) * 128 + ((g) & 3) * 16) * DM; \
;         _Pragma("unroll") for (int bj_ = 0; bj_ < 2; ++bj_) { dst[bj_][0] = *(const f32x4*)(X + off_ + bj_ * 128); dst[bj_][1] = *(const f32x4*)(X + off_ + bj_ * 128 + (size_t)8 * DM); } } while (0)
;     __device__ __forceinline__ void operator()(const f32x4 (&acc)[2][2][4][2], const pg8::Unit& u, const Pre&, int wr, int wc, int fr, int fq) const {
;         const int lane = fr | (fq << 4), rr = lane >> 3, pc = lane & 7;
;         LAS unsigned char* slab = scr + (wr * 4 + wc) * 2048;
;         LAS unsigned char* wp0 = slab + fr * 128 + (((2 * fq) ^ (fr & 7)) << 4); LAS unsigned char* wp1 = slab + fr * 128 + (((2 * fq + 1) ^ (fr & 7)) << 4);
;         const LAS unsigned char* rp0 = slab + rr * 128 + ((pc ^ (rr & 7)) << 4); const LAS unsigned char* rp1 = rp0 + 1024;
;         const size_t base = (size_t)(u.pm * 256 + wr * 64 + rr) * DM + u.pn * 256 + wc * 32 + 4 * pc;
;         f32x4 xa[2][2], xb[2][2];
;     ...
;         EPO_LOAD(xa, 0);
;         EPO_LOAD(xb, 1); __builtin_amdgcn_sched_barrier(0); EPO_DO(xa, 0); __builtin_amdgcn_sched_barrier(0);
;         EPO_LOAD(xa, 2); __builtin_amdgcn_sched_barrier(0); EPO_DO(xb, 1); __builtin_amdgcn_sched_barrier(0);
;         EPO_LOAD(xb, 3); __builtin_amdgcn_sched_barrier(0); EPO_DO(xa, 2); __builtin_amdgcn_sched_barrier(0);
;         EPO_LOAD(xa, 4); __builtin_amdgcn_sched_barrier(0); EPO_DO(xb, 3); __builtin_amdgcn_sched_barrier(0);
;         EPO_LOAD(xb, 5); __builtin_amdgcn_sched_barrier(0); EPO_DO(xa, 4); __builtin_amdgcn_sched_barrier(0);
;         EPO_LOAD(xa, 6); __builtin_amdgcn_sched_barrier(0); EPO_DO(xb, 5); __builtin_amdgcn_sched_barrier(0);
;         EPO_LOAD(xb, 7); __builtin_amdgcn_sched_barrier(0); EPO_DO(xa, 6); __builtin_amdgcn_sched_barrier(0);
;         EPO_DO(xb, 7);
	s_add_i32 s79, s79, 2
	s_addk_i32 s77, 0x100
	s_addk_i32 s78, 0x100
	s_cmp_gt_u32 s79, 29
	s_cbranch_scc0 .LBB0_708
	s_mov_b32 s10, 0
	s_mov_b32 s11, 0
	s_nop 15
	s_nop 3
	v_mov_b32_e32 v154, v0
	v_readlane_b32 s80, v245, 21
	v_readfirstlane_b32 s10, v154
	s_ashr_i32 s75, s10, 8
	s_bfe_u32 s76, s10, 0x20006
	s_lshl_b32 s10, s74, 8
	s_lshl_b32 s11, s75, 6
	v_bfe_u32 v155, v154, 3, 3
	s_add_i32 s11, s11, s10
	v_or_b32_e32 v130, s11, v155
	v_ashrrev_i32_e32 v131, 31, v130
	s_lshl_b32 s10, s33, 8
	v_and_b32_e32 v177, 7, v154
	v_lshlrev_b64 v[130:131], 11, v[130:131]
	s_ashr_i32 s11, s10, 31
	v_lshl_add_u64 v[160:161], v[130:131], 0, s[10:11]
	s_lshl_b32 s10, s76, 5
	v_lshlrev_b32_e32 v130, 2, v177
	v_or3_b32 v160, v160, s10, v130
	v_lshlrev_b64 v[186:187], 2, v[160:161]
	v_readlane_b32 s81, v245, 22
	s_lshl_b32 s10, s75, 13
	s_lshl_b32 s11, s76, 11
	v_lshl_add_u64 v[150:151], s[80:81], 0, v[186:187]
	v_add_co_u32_e32 v130, vcc, s45, v150
	s_add_i32 s10, s10, 0
	s_nop 0
	v_addc_co_u32_e32 v131, vcc, 0, v151, vcc
	v_add_co_u32_e32 v132, vcc, s7, v150
	global_load_dwordx4 v[146:149], v[150:151], off
	global_load_dwordx4 v[156:159], v[150:151], off offset:512
	global_load_dwordx4 v[178:181], v[130:131], off
	global_load_dwordx4 v[182:185], v[130:131], off offset:512
	v_addc_co_u32_e32 v133, vcc, 0, v151, vcc
	v_lshl_add_u64 v[130:131], v[150:151], 0, s[16:17]
	v_add_co_u32_e32 v152, vcc, s57, v150
	s_add_i32 s10, s10, s11
	s_nop 0
	v_addc_co_u32_e32 v153, vcc, 0, v151, vcc
	global_load_dwordx4 v[142:145], v[132:133], off
	global_load_dwordx4 v[134:137], v[130:131], off offset:512
	global_load_dwordx4 v[138:141], v[152:153], off
	s_nop 0
	global_load_dwordx4 v[130:133], v[152:153], off offset:512
	v_lshrrev_b32_e32 v152, 3, v154
	v_lshlrev_b32_e32 v153, 7, v154
	s_add_i32 s10, s10, 0x20000
	v_and_b32_e32 v153, 0x780, v153
	v_and_b32_e32 v188, 6, v152
	v_bitop3_b32 v189, v152, v177, 6 bitop3:0x6c
	v_bitop3_b32 v152, v152, v154, 7 bitop3:0x28
	v_readlane_b32 s82, v245, 23
	v_readlane_b32 s83, v245, 24
	v_readlane_b32 s94, v245, 35
	v_bitop3_b32 v177, v188, v177, 1 bitop3:0x36
	v_lshlrev_b32_e32 v155, 7, v155
	v_lshlrev_b32_e32 v152, 4, v152
	v_add_u32_e32 v154, s10, v153
	v_readlane_b32 s84, v245, 25
	v_readlane_b32 s85, v245, 26
	v_readlane_b32 s86, v245, 27
	v_readlane_b32 s87, v245, 28
	v_readlane_b32 s88, v245, 29
	v_readlane_b32 s89, v245, 30
	v_readlane_b32 s90, v245, 31
	v_readlane_b32 s91, v245, 32
	v_readlane_b32 s92, v245, 33
	v_readlane_b32 s93, v245, 34
	v_readlane_b32 s95, v245, 36
	v_add3_u32 v152, s10, v155, v152
	v_lshl_add_u32 v153, v177, 4, v154
	v_lshl_add_u32 v154, v189, 4, v154
	ds_write_b128 v154, v[126:129]
	ds_write_b128 v153, v[122:125]
	ds_read_b128 v[122:125], v152
	ds_read_b128 v[126:129], v152 offset:1024
	v_mov_b32_e32 v155, 0
	s_movk_i32 s10, 0x4000
	s_waitcnt vmcnt(7) lgkmcnt(1)
	v_pk_add_f32 v[122:123], v[146:147], v[122:123]
	s_nop 0
	v_cvt_pk_fp8_f32 v155, v122, v123
	v_pk_add_f32 v[124:125], v[148:149], v[124:125]
	v_lshl_add_u64 v[148:149], s[12:13], 0, v[186:187]
	s_waitcnt vmcnt(5) lgkmcnt(0)
	v_pk_add_f32 v[126:127], v[178:179], v[126:127]
	global_store_dwordx4 v[148:149], v[122:125], off
	v_cvt_pk_fp8_f32 v155, v124, v125 op_sel:[0,0,1]
	v_pk_add_f32 v[128:129], v[180:181], v[128:129]
	v_mov_b32_e32 v124, 0
	v_cvt_pk_fp8_f32 v124, v126, v127
	v_add_co_u32_e32 v178, vcc, s45, v148
	v_lshl_add_u64 v[146:147], s[14:15], 0, v[160:161]
	v_cvt_pk_fp8_f32 v124, v128, v129 op_sel:[0,0,1]
	v_addc_co_u32_e32 v179, vcc, 0, v149, vcc
	v_add_co_u32_e32 v122, vcc, s10, v146
	global_store_dwordx4 v[178:179], v[126:129], off
	s_nop 0
	v_addc_co_u32_e32 v123, vcc, 0, v147, vcc
	global_store_dword v[146:147], v155, off
	global_store_dword v[122:123], v124, off
	ds_write_b128 v154, v[118:121]
	ds_write_b128 v153, v[114:117]
	ds_read_b128 v[114:117], v152
	ds_read_b128 v[118:121], v152 offset:1024
	v_mov_b32_e32 v124, 0
	s_waitcnt lgkmcnt(1)
	v_pk_add_f32 v[116:117], v[158:159], v[116:117]
	v_pk_add_f32 v[114:115], v[156:157], v[114:115]
	s_waitcnt vmcnt(8) lgkmcnt(0)
	v_pk_add_f32 v[120:121], v[184:185], v[120:121]
	v_pk_add_f32 v[118:119], v[182:183], v[118:119]
	global_store_dwordx4 v[148:149], v[114:117], off offset:512
	global_store_dwordx4 v[178:179], v[118:121], off offset:512
	v_cvt_pk_fp8_f32 v124, v114, v115
	v_mov_b32_e32 v114, 0
	v_cvt_pk_fp8_f32 v114, v118, v119
	v_cvt_pk_fp8_f32 v124, v116, v117 op_sel:[0,0,1]
	v_cvt_pk_fp8_f32 v114, v120, v121 op_sel:[0,0,1]
	global_store_dword v[146:147], v124, off offset:128
	global_store_dword v[122:123], v114, off offset:128
	v_add_co_u32_e32 v116, vcc, s58, v150
	v_lshl_add_u64 v[114:115], v[150:151], 0, s[18:19]
	s_nop 0
	v_addc_co_u32_e32 v117, vcc, 0, v151, vcc
	v_add_co_u32_e32 v156, vcc, s59, v150
	s_nop 1
	v_addc_co_u32_e32 v157, vcc, 0, v151, vcc
	global_load_dwordx4 v[126:129], v[116:117], off
	global_load_dwordx4 v[118:121], v[114:115], off offset:512
	global_load_dwordx4 v[122:125], v[156:157], off
	s_nop 0
	global_load_dwordx4 v[114:117], v[156:157], off offset:512
	ds_write_b128 v154, v[110:113]
	ds_write_b128 v153, v[106:109]
	ds_read_b128 v[106:109], v152
	ds_read_b128 v[110:113], v152 offset:1024
	s_mov_b64 s[10:11], 0x8000
	s_waitcnt vmcnt(15) lgkmcnt(1)
	v_pk_add_f32 v[106:107], v[142:143], v[106:107]
	v_mov_b32_e32 v142, 0
	v_cvt_pk_fp8_f32 v142, v106, v107
	s_waitcnt vmcnt(13) lgkmcnt(0)
; #define EPO_LOAD(dst, g) do { const size_t off_ = base + (size_t)(((g) >> 2) * 128 + ((g) & 3) * 16) * DM; \
;         _Pragma("unroll") for (int bj_ = 0; bj_ < 2; ++bj_) { dst[bj_][0] = *(const f32x4*)(X + off_ + bj_ * 128); dst[bj_][1] = *(const f32x4*)(X + off_ + bj_ * 128 + (size_t)8 * DM); } } while (0)
;     __device__ __forceinline__ void operator()(const f32x4 (&acc)[2][2][4][2], const pg8::Unit& u, const Pre&, int wr, int wc, int fr, int fq) const {
;     ...
;         EPO_LOAD(xa, 0);
;         EPO_LOAD(xb, 1); __builtin_amdgcn_sched_barrier(0); EPO_DO(xa, 0); __builtin_amdgcn_sched_barrier(0);
;         EPO_LOAD(xa, 2); __builtin_amdgcn_sched_barrier(0); EPO_DO(xb, 1); __builtin_amdgcn_sched_barrier(0);
;         EPO_LOAD(xb, 3); __builtin_amdgcn_sched_barrier(0); EPO_DO(xa, 2); __builtin_amdgcn_sched_barrier(0);
	v_pk_add_f32 v[112:113], v[140:141], v[112:113]
	v_add_co_u32_e32 v140, vcc, s7, v148
	v_pk_add_f32 v[108:109], v[144:145], v[108:109]
	s_nop 0
	v_addc_co_u32_e32 v141, vcc, 0, v149, vcc
	global_store_dwordx4 v[140:141], v[106:109], off
	v_add_co_u32_e32 v140, vcc, s57, v148
	v_cvt_pk_fp8_f32 v142, v108, v109 op_sel:[0,0,1]
	s_nop 0
	v_addc_co_u32_e32 v141, vcc, 0, v149, vcc
	v_lshl_add_u64 v[106:107], v[146:147], 0, s[10:11]
	s_mov_b32 s10, 0x8000
	v_add_co_u32_e32 v108, vcc, s10, v146
	v_pk_add_f32 v[110:111], v[138:139], v[110:111]
	s_nop 0
	v_addc_co_u32_e32 v109, vcc, 0, v147, vcc
	global_store_dwordx4 v[140:141], v[110:113], off
	global_store_dword v[108:109], v142, off
	v_mov_b32_e32 v142, 0
	v_cvt_pk_fp8_f32 v142, v110, v111
	s_mov_b32 s10, 0xc000
	v_add_co_u32_e32 v108, vcc, s10, v146
	v_cvt_pk_fp8_f32 v142, v112, v113 op_sel:[0,0,1]
	s_nop 0
	v_addc_co_u32_e32 v109, vcc, 0, v147, vcc
	v_lshl_add_u64 v[138:139], v[148:149], 0, s[16:17]
	global_store_dword v[108:109], v142, off
	ds_write_b128 v154, v[102:105]
	ds_write_b128 v153, v[98:101]
	ds_read_b128 v[98:101], v152
	ds_read_b128 v[102:105], v152 offset:1024
	v_mov_b32_e32 v110, 0
	s_waitcnt lgkmcnt(1)
	v_pk_add_f32 v[100:101], v[136:137], v[100:101]
	v_pk_add_f32 v[98:99], v[134:135], v[98:99]
	s_waitcnt vmcnt(16) lgkmcnt(0)
	v_pk_add_f32 v[104:105], v[132:133], v[104:105]
	v_pk_add_f32 v[102:103], v[130:131], v[102:103]
	global_store_dwordx4 v[138:139], v[98:101], off offset:512
	global_store_dwordx4 v[140:141], v[102:105], off offset:512
	v_cvt_pk_fp8_f32 v110, v98, v99
	v_mov_b32_e32 v98, 0
	v_cvt_pk_fp8_f32 v98, v102, v103
	v_cvt_pk_fp8_f32 v110, v100, v101 op_sel:[0,0,1]
	v_cvt_pk_fp8_f32 v98, v104, v105 op_sel:[0,0,1]
	global_store_dword v[106:107], v110, off offset:128
	global_store_dword v[108:109], v98, off offset:128
	v_add_co_u32_e32 v100, vcc, s60, v150
	v_lshl_add_u64 v[98:99], v[150:151], 0, s[20:21]
	s_nop 0
	v_addc_co_u32_e32 v101, vcc, 0, v151, vcc
	v_add_co_u32_e32 v130, vcc, s61, v150
	s_nop 1
	v_addc_co_u32_e32 v131, vcc, 0, v151, vcc
	global_load_dwordx4 v[110:113], v[100:101], off
	global_load_dwordx4 v[102:105], v[98:99], off offset:512
	global_load_dwordx4 v[106:109], v[130:131], off
	s_nop 0
	global_load_dwordx4 v[98:101], v[130:131], off offset:512
	ds_write_b128 v154, v[94:97]
	ds_write_b128 v153, v[90:93]
	ds_read_b128 v[90:93], v152
	ds_read_b128 v[94:97], v152 offset:1024
	s_mov_b64 s[10:11], 0x10000
	s_waitcnt vmcnt(15) lgkmcnt(1)
	v_pk_add_f32 v[90:91], v[126:127], v[90:91]
	v_mov_b32_e32 v126, 0
	v_cvt_pk_fp8_f32 v126, v90, v91
	s_waitcnt vmcnt(13) lgkmcnt(0)
	v_pk_add_f32 v[96:97], v[124:125], v[96:97]
	v_add_co_u32_e32 v124, vcc, s58, v148
	v_pk_add_f32 v[92:93], v[128:129], v[92:93]
	s_nop 0
	v_addc_co_u32_e32 v125, vcc, 0, v149, vcc
	global_store_dwordx4 v[124:125], v[90:93], off
	v_add_co_u32_e32 v124, vcc, s59, v148
	v_cvt_pk_fp8_f32 v126, v92, v93 op_sel:[0,0,1]
	s_nop 0
	v_addc_co_u32_e32 v125, vcc, 0, v149, vcc
	v_add_co_u32_e32 v92, vcc, s45, v146
	v_pk_add_f32 v[94:95], v[122:123], v[94:95]
	s_nop 0
	v_addc_co_u32_e32 v93, vcc, 0, v147, vcc
	global_store_dwordx4 v[124:125], v[94:97], off
	global_store_dword v[92:93], v126, off
	v_mov_b32_e32 v126, 0
	v_cvt_pk_fp8_f32 v126, v94, v95
	v_lshl_add_u64 v[90:91], v[146:147], 0, s[10:11]
	s_mov_b32 s10, 0x14000
	v_add_co_u32_e32 v92, vcc, s10, v146
	v_cvt_pk_fp8_f32 v126, v96, v97 op_sel:[0,0,1]
	s_nop 0
	v_addc_co_u32_e32 v93, vcc, 0, v147, vcc
	v_lshl_add_u64 v[122:123], v[148:149], 0, s[18:19]
	global_store_dword v[92:93], v126, off
	ds_write_b128 v154, v[86:89]
	ds_write_b128 v153, v[82:85]
	ds_read_b128 v[82:85], v152
	ds_read_b128 v[86:89], v152 offset:1024
	v_mov_b32_e32 v94, 0
	s_waitcnt lgkmcnt(1)
	v_pk_add_f32 v[84:85], v[120:121], v[84:85]
	v_pk_add_f32 v[82:83], v[118:119], v[82:83]
	s_waitcnt vmcnt(16) lgkmcnt(0)
	v_pk_add_f32 v[88:89], v[116:117], v[88:89]
	v_pk_add_f32 v[86:87], v[114:115], v[86:87]
	global_store_dwordx4 v[122:123], v[82:85], off offset:512
	global_store_dwordx4 v[124:125], v[86:89], off offset:512
	v_cvt_pk_fp8_f32 v94, v82, v83
	v_mov_b32_e32 v82, 0
	v_cvt_pk_fp8_f32 v82, v86, v87
	v_cvt_pk_fp8_f32 v94, v84, v85 op_sel:[0,0,1]
	v_cvt_pk_fp8_f32 v82, v88, v89 op_sel:[0,0,1]
	global_store_dword v[90:91], v94, off offset:128
	global_store_dword v[92:93], v82, off offset:128
	v_add_co_u32_e32 v84, vcc, s62, v150
	v_lshl_add_u64 v[82:83], v[150:151], 0, s[22:23]
	s_nop 0
	v_addc_co_u32_e32 v85, vcc, 0, v151, vcc
	v_add_co_u32_e32 v114, vcc, s63, v150
	s_nop 1
	v_addc_co_u32_e32 v115, vcc, 0, v151, vcc
	global_load_dwordx4 v[94:97], v[84:85], off
	global_load_dwordx4 v[86:89], v[82:83], off offset:512
	global_load_dwordx4 v[90:93], v[114:115], off
	s_nop 0
	global_load_dwordx4 v[82:85], v[114:115], off offset:512
	ds_write_b128 v154, v[78:81]
	ds_write_b128 v153, v[74:77]
	ds_read_b128 v[74:77], v152
	ds_read_b128 v[78:81], v152 offset:1024
	s_mov_b64 s[10:11], 0x18000
	s_waitcnt vmcnt(15) lgkmcnt(1)
	v_pk_add_f32 v[74:75], v[110:111], v[74:75]
	v_mov_b32_e32 v110, 0
	v_cvt_pk_fp8_f32 v110, v74, v75
	s_waitcnt vmcnt(13) lgkmcnt(0)
; #define EPO_LOAD(dst, g) do { const size_t off_ = base + (size_t)(((g) >> 2) * 128 + ((g) & 3) * 16) * DM; \
;         _Pragma("unroll") for (int bj_ = 0; bj_ < 2; ++bj_) { dst[bj_][0] = *(const f32x4*)(X + off_ + bj_ * 128); dst[bj_][1] = *(const f32x4*)(X + off_ + bj_ * 128 + (size_t)8 * DM); } } while (0)
;     __device__ __forceinline__ void operator()(const f32x4 (&acc)[2][2][4][2], const pg8::Unit& u, const Pre&, int wr, int wc, int fr, int fq) const {
;     ...
;         EPO_LOAD(xa, 0);
;         EPO_LOAD(xb, 1); __builtin_amdgcn_sched_barrier(0); EPO_DO(xa, 0); __builtin_amdgcn_sched_barrier(0);
;         EPO_LOAD(xa, 2); __builtin_amdgcn_sched_barrier(0); EPO_DO(xb, 1); __builtin_amdgcn_sched_barrier(0);
;         EPO_LOAD(xb, 3); __builtin_amdgcn_sched_barrier(0); EPO_DO(xa, 2); __builtin_amdgcn_sched_barrier(0);
	v_pk_add_f32 v[80:81], v[108:109], v[80:81]
	v_add_co_u32_e32 v108, vcc, s60, v148
	v_pk_add_f32 v[76:77], v[112:113], v[76:77]
	s_nop 0
	v_addc_co_u32_e32 v109, vcc, 0, v149, vcc
	global_store_dwordx4 v[108:109], v[74:77], off
	v_add_co_u32_e32 v108, vcc, s61, v148
	v_cvt_pk_fp8_f32 v110, v76, v77 op_sel:[0,0,1]
	s_nop 0
	v_addc_co_u32_e32 v109, vcc, 0, v149, vcc
	v_lshl_add_u64 v[74:75], v[146:147], 0, s[10:11]
	s_mov_b32 s10, 0x18000
	v_add_co_u32_e32 v76, vcc, s10, v146
	v_pk_add_f32 v[78:79], v[106:107], v[78:79]
	s_nop 0
	v_addc_co_u32_e32 v77, vcc, 0, v147, vcc
	global_store_dwordx4 v[108:109], v[78:81], off
	global_store_dword v[76:77], v110, off
	v_mov_b32_e32 v110, 0
	v_cvt_pk_fp8_f32 v110, v78, v79
	s_mov_b32 s10, 0x1c000
	v_add_co_u32_e32 v76, vcc, s10, v146
	v_cvt_pk_fp8_f32 v110, v80, v81 op_sel:[0,0,1]
	s_nop 0
	v_addc_co_u32_e32 v77, vcc, 0, v147, vcc
	v_lshl_add_u64 v[106:107], v[148:149], 0, s[20:21]
	global_store_dword v[76:77], v110, off
	ds_write_b128 v154, v[70:73]
	ds_write_b128 v153, v[66:69]
	ds_read_b128 v[66:69], v152
	ds_read_b128 v[70:73], v152 offset:1024
	v_mov_b32_e32 v78, 0
	s_waitcnt lgkmcnt(1)
	v_pk_add_f32 v[68:69], v[104:105], v[68:69]
	v_pk_add_f32 v[66:67], v[102:103], v[66:67]
	s_waitcnt vmcnt(16) lgkmcnt(0)
	v_pk_add_f32 v[72:73], v[100:101], v[72:73]
	v_pk_add_f32 v[70:71], v[98:99], v[70:71]
	global_store_dwordx4 v[106:107], v[66:69], off offset:512
	global_store_dwordx4 v[108:109], v[70:73], off offset:512
	v_cvt_pk_fp8_f32 v78, v66, v67
	v_mov_b32_e32 v66, 0
	v_cvt_pk_fp8_f32 v66, v70, v71
	v_cvt_pk_fp8_f32 v78, v68, v69 op_sel:[0,0,1]
	v_cvt_pk_fp8_f32 v66, v72, v73 op_sel:[0,0,1]
	global_store_dword v[74:75], v78, off offset:128
	global_store_dword v[76:77], v66, off offset:128
	v_add_co_u32_e32 v68, vcc, s64, v150
	v_lshl_add_u64 v[66:67], v[150:151], 0, s[24:25]
	s_nop 0
	v_addc_co_u32_e32 v69, vcc, 0, v151, vcc
	v_add_co_u32_e32 v98, vcc, s65, v150
	s_nop 1
	v_addc_co_u32_e32 v99, vcc, 0, v151, vcc
	global_load_dwordx4 v[78:81], v[68:69], off
	global_load_dwordx4 v[70:73], v[66:67], off offset:512
	global_load_dwordx4 v[74:77], v[98:99], off
	s_nop 0
	global_load_dwordx4 v[66:69], v[98:99], off offset:512
	ds_write_b128 v154, v[62:65]
	ds_write_b128 v153, v[58:61]
	ds_read_b128 v[58:61], v152
	ds_read_b128 v[62:65], v152 offset:1024
	s_mov_b32 s10, 0x44000
	s_waitcnt vmcnt(15) lgkmcnt(1)
	v_pk_add_f32 v[58:59], v[94:95], v[58:59]
	v_mov_b32_e32 v94, 0
	v_cvt_pk_fp8_f32 v94, v58, v59
	s_waitcnt vmcnt(13) lgkmcnt(0)
	v_pk_add_f32 v[64:65], v[92:93], v[64:65]
	v_add_co_u32_e32 v92, vcc, s62, v148
	v_pk_add_f32 v[60:61], v[96:97], v[60:61]
	s_nop 0
	v_addc_co_u32_e32 v93, vcc, 0, v149, vcc
	global_store_dwordx4 v[92:93], v[58:61], off
	v_add_co_u32_e32 v92, vcc, s63, v148
	v_cvt_pk_fp8_f32 v94, v60, v61 op_sel:[0,0,1]
	s_nop 0
	v_addc_co_u32_e32 v93, vcc, 0, v149, vcc
	v_add_co_u32_e32 v60, vcc, s58, v146
	v_pk_add_f32 v[62:63], v[90:91], v[62:63]
	s_nop 0
	v_addc_co_u32_e32 v61, vcc, 0, v147, vcc
	global_store_dwordx4 v[92:93], v[62:65], off
	global_store_dword v[60:61], v94, off
	v_mov_b32_e32 v94, 0
	v_cvt_pk_fp8_f32 v94, v62, v63
	v_add_co_u32_e32 v60, vcc, s10, v146
	v_lshl_add_u64 v[90:91], v[148:149], 0, s[22:23]
	v_cvt_pk_fp8_f32 v94, v64, v65 op_sel:[0,0,1]
	v_addc_co_u32_e32 v61, vcc, 0, v147, vcc
	v_mov_b32_e32 v62, 0
	global_store_dword v[60:61], v94, off
	ds_write_b128 v154, v[54:57]
	ds_write_b128 v153, v[50:53]
	ds_read_b128 v[50:53], v152
	ds_read_b128 v[54:57], v152 offset:1024
	v_lshl_add_u64 v[58:59], v[146:147], 0, s[18:19]
	s_waitcnt lgkmcnt(1)
	v_pk_add_f32 v[52:53], v[88:89], v[52:53]
	v_pk_add_f32 v[50:51], v[86:87], v[50:51]
	s_waitcnt vmcnt(16) lgkmcnt(0)
	v_pk_add_f32 v[56:57], v[84:85], v[56:57]
	v_pk_add_f32 v[54:55], v[82:83], v[54:55]
	global_store_dwordx4 v[90:91], v[50:53], off offset:512
	global_store_dwordx4 v[92:93], v[54:57], off offset:512
	v_cvt_pk_fp8_f32 v62, v50, v51
	v_mov_b32_e32 v50, 0
	v_cvt_pk_fp8_f32 v50, v54, v55
	v_cvt_pk_fp8_f32 v62, v52, v53 op_sel:[0,0,1]
	v_cvt_pk_fp8_f32 v50, v56, v57 op_sel:[0,0,1]
	global_store_dword v[58:59], v62, off offset:128
	global_store_dword v[60:61], v50, off offset:128
	v_add_co_u32_e32 v52, vcc, s66, v150
	v_lshl_add_u64 v[50:51], v[150:151], 0, s[26:27]
	s_nop 0
	v_addc_co_u32_e32 v53, vcc, 0, v151, vcc
	v_add_co_u32_e32 v82, vcc, s67, v150
	s_nop 1
	v_addc_co_u32_e32 v83, vcc, 0, v151, vcc
	global_load_dwordx4 v[62:65], v[52:53], off
	global_load_dwordx4 v[54:57], v[50:51], off offset:512
	global_load_dwordx4 v[58:61], v[82:83], off
	s_nop 0
	global_load_dwordx4 v[50:53], v[82:83], off offset:512
	ds_write_b128 v154, v[46:49]
	ds_write_b128 v153, v[42:45]
	ds_read_b128 v[42:45], v152
	ds_read_b128 v[46:49], v152 offset:1024
	s_mov_b64 s[10:11], 0x48000
	s_waitcnt vmcnt(15) lgkmcnt(1)
	v_pk_add_f32 v[42:43], v[78:79], v[42:43]
	v_mov_b32_e32 v78, 0
	v_cvt_pk_fp8_f32 v78, v42, v43
	s_waitcnt vmcnt(13) lgkmcnt(0)
	v_pk_add_f32 v[48:49], v[76:77], v[48:49]
	v_add_co_u32_e32 v76, vcc, s64, v148
	v_pk_add_f32 v[44:45], v[80:81], v[44:45]
	s_nop 0
	v_addc_co_u32_e32 v77, vcc, 0, v149, vcc
	global_store_dwordx4 v[76:77], v[42:45], off
	v_add_co_u32_e32 v76, vcc, s65, v148
	v_cvt_pk_fp8_f32 v78, v44, v45 op_sel:[0,0,1]
	s_nop 0
	v_addc_co_u32_e32 v77, vcc, 0, v149, vcc
	v_lshl_add_u64 v[42:43], v[146:147], 0, s[10:11]
	s_mov_b32 s10, 0x48000
	v_add_co_u32_e32 v44, vcc, s10, v146
	v_pk_add_f32 v[46:47], v[74:75], v[46:47]
	s_nop 0
	v_addc_co_u32_e32 v45, vcc, 0, v147, vcc
	global_store_dwordx4 v[76:77], v[46:49], off
	global_store_dword v[44:45], v78, off
	v_mov_b32_e32 v78, 0
	v_cvt_pk_fp8_f32 v78, v46, v47
	s_mov_b32 s10, 0x4c000
	v_add_co_u32_e32 v44, vcc, s10, v146
	v_cvt_pk_fp8_f32 v78, v48, v49 op_sel:[0,0,1]
	s_nop 0
	v_addc_co_u32_e32 v45, vcc, 0, v147, vcc
	v_lshl_add_u64 v[74:75], v[148:149], 0, s[24:25]
	global_store_dword v[44:45], v78, off
	ds_write_b128 v154, v[38:41]
	ds_write_b128 v153, v[34:37]
	ds_read_b128 v[34:37], v152
	ds_read_b128 v[38:41], v152 offset:1024
	v_mov_b32_e32 v46, 0
	s_waitcnt lgkmcnt(1)
; #define PG8_WAIT_V(n) asm volatile("s_waitcnt vmcnt(" #n ")" ::: "memory")
; #define PG8_BAR __builtin_amdgcn_s_barrier()
; #define EPO_LOAD(dst, g) do { const size_t off_ = base + (size_t)(((g) >> 2) * 128 + ((g) & 3) * 16) * DM; \
;         _Pragma("unroll") for (int bj_ = 0; bj_ < 2; ++bj_) { dst[bj_][0] = *(const f32x4*)(X + off_ + bj_ * 128); dst[bj_][1] = *(const f32x4*)(X + off_ + bj_ * 128 + (size_t)8 * DM); } } while (0)
; template <class Epi, class Sched, bool GATHER, bool ALIGN_EPI, bool SP2, bool FP8>
; __device__ __forceinline__ void gemm_phase(LAS unsigned char* lds, const Gemm g, const Sched& S, const Epi& E) {
;     ...
;         if (!has_next) break;
; #pragma unroll
;         for (int a = 0; a < 2; ++a)
; #pragma unroll
;             for (int b = 0; b < 2; ++b)
; #pragma unroll
;                 for (int m = 0; m < 4; ++m)
; #pragma unroll
;                     for (int n = 0; n < 2; ++n) acc[a][b][m][n] = (f32x4){0.f, 0.f, 0.f, 0.f};
;         cur = nxt; cA = nA; cB = nB; ++ui;
;         vA0 = nvA0; vA1 = nvA1;
;         if constexpr (ALIGN_EPI) { if (wr == 1) PG8_BAR; }
;     }
;     PG8_WAIT_V(0);
;     if constexpr (!ALIGN_EPI) { if (wr == 0) PG8_BAR; }
;     PG8_BAR;
;     __device__ __forceinline__ void operator()(const f32x4 (&acc)[2][2][4][2], const pg8::Unit& u, const Pre&, int wr, int wc, int fr, int fq) const {
;     ...
;         EPO_LOAD(xa, 0);
;         EPO_LOAD(xb, 1); __builtin_amdgcn_sched_barrier(0); EPO_DO(xa, 0); __builtin_amdgcn_sched_barrier(0);
;         EPO_LOAD(xa, 2); __builtin_amdgcn_sched_barrier(0); EPO_DO(xb, 1); __builtin_amdgcn_sched_barrier(0);
;         EPO_LOAD(xb, 3); __builtin_amdgcn_sched_barrier(0); EPO_DO(xa, 2); __builtin_amdgcn_sched_barrier(0);
;         EPO_LOAD(xa, 4); __builtin_amdgcn_sched_barrier(0); EPO_DO(xb, 3); __builtin_amdgcn_sched_barrier(0);
;         EPO_LOAD(xb, 5); __builtin_amdgcn_sched_barrier(0); EPO_DO(xa, 4); __builtin_amdgcn_sched_barrier(0);
;         EPO_LOAD(xa, 6); __builtin_amdgcn_sched_barrier(0); EPO_DO(xb, 5); __builtin_amdgcn_sched_barrier(0);
;         EPO_LOAD(xb, 7); __builtin_amdgcn_sched_barrier(0); EPO_DO(xa, 6); __builtin_amdgcn_sched_barrier(0);
;         EPO_DO(xb, 7);
	v_pk_add_f32 v[36:37], v[72:73], v[36:37]
	v_pk_add_f32 v[34:35], v[70:71], v[34:35]
	s_waitcnt vmcnt(16) lgkmcnt(0)
	v_pk_add_f32 v[40:41], v[68:69], v[40:41]
	v_pk_add_f32 v[38:39], v[66:67], v[38:39]
	global_store_dwordx4 v[74:75], v[34:37], off offset:512
	global_store_dwordx4 v[76:77], v[38:41], off offset:512
	v_cvt_pk_fp8_f32 v46, v34, v35
	v_mov_b32_e32 v34, 0
	v_cvt_pk_fp8_f32 v34, v38, v39
	v_cvt_pk_fp8_f32 v46, v36, v37 op_sel:[0,0,1]
	v_cvt_pk_fp8_f32 v34, v40, v41 op_sel:[0,0,1]
	global_store_dword v[42:43], v46, off offset:128
	global_store_dword v[44:45], v34, off offset:128
	v_add_co_u32_e32 v36, vcc, s68, v150
	v_lshl_add_u64 v[34:35], v[150:151], 0, s[28:29]
	s_nop 0
	v_addc_co_u32_e32 v37, vcc, 0, v151, vcc
	v_add_co_u32_e32 v66, vcc, s69, v150
	s_nop 1
	v_addc_co_u32_e32 v67, vcc, 0, v151, vcc
	global_load_dwordx4 v[46:49], v[36:37], off
	global_load_dwordx4 v[38:41], v[34:35], off offset:512
	global_load_dwordx4 v[42:45], v[66:67], off
	s_nop 0
	global_load_dwordx4 v[34:37], v[66:67], off offset:512
	ds_write_b128 v154, v[30:33]
	ds_write_b128 v153, v[26:29]
	ds_read_b128 v[26:29], v152
	ds_read_b128 v[30:33], v152 offset:1024
	s_mov_b64 s[10:11], 0x50000
	s_waitcnt vmcnt(15) lgkmcnt(1)
	v_pk_add_f32 v[26:27], v[62:63], v[26:27]
	v_mov_b32_e32 v62, 0
	v_cvt_pk_fp8_f32 v62, v26, v27
	s_waitcnt vmcnt(13) lgkmcnt(0)
	v_pk_add_f32 v[32:33], v[60:61], v[32:33]
	v_add_co_u32_e32 v60, vcc, s66, v148
	v_pk_add_f32 v[28:29], v[64:65], v[28:29]
	s_nop 0
	v_addc_co_u32_e32 v61, vcc, 0, v149, vcc
	global_store_dwordx4 v[60:61], v[26:29], off
	v_add_co_u32_e32 v60, vcc, s67, v148
	v_cvt_pk_fp8_f32 v62, v28, v29 op_sel:[0,0,1]
	s_nop 0
	v_addc_co_u32_e32 v61, vcc, 0, v149, vcc
	v_add_co_u32_e32 v28, vcc, s59, v146
	v_pk_add_f32 v[30:31], v[58:59], v[30:31]
	s_nop 0
	v_addc_co_u32_e32 v29, vcc, 0, v147, vcc
	global_store_dwordx4 v[60:61], v[30:33], off
	global_store_dword v[28:29], v62, off
	v_mov_b32_e32 v62, 0
	v_cvt_pk_fp8_f32 v62, v30, v31
	v_lshl_add_u64 v[26:27], v[146:147], 0, s[10:11]
	s_mov_b32 s10, 0x54000
	v_add_co_u32_e32 v28, vcc, s10, v146
	v_cvt_pk_fp8_f32 v62, v32, v33 op_sel:[0,0,1]
	s_nop 0
	v_addc_co_u32_e32 v29, vcc, 0, v147, vcc
	v_lshl_add_u64 v[58:59], v[148:149], 0, s[26:27]
	global_store_dword v[28:29], v62, off
	ds_write_b128 v154, v[22:25]
	ds_write_b128 v153, v[18:21]
	ds_read_b128 v[18:21], v152
	ds_read_b128 v[22:25], v152 offset:1024
	v_mov_b32_e32 v30, 0
	s_waitcnt lgkmcnt(1)
	v_pk_add_f32 v[20:21], v[56:57], v[20:21]
	v_pk_add_f32 v[18:19], v[54:55], v[18:19]
	s_waitcnt vmcnt(16) lgkmcnt(0)
	v_pk_add_f32 v[24:25], v[52:53], v[24:25]
	v_pk_add_f32 v[22:23], v[50:51], v[22:23]
	global_store_dwordx4 v[58:59], v[18:21], off offset:512
	global_store_dwordx4 v[60:61], v[22:25], off offset:512
	v_cvt_pk_fp8_f32 v30, v18, v19
	v_mov_b32_e32 v18, 0
	v_cvt_pk_fp8_f32 v18, v22, v23
	v_cvt_pk_fp8_f32 v30, v20, v21 op_sel:[0,0,1]
	v_cvt_pk_fp8_f32 v18, v24, v25 op_sel:[0,0,1]
	global_store_dword v[26:27], v30, off offset:128
	global_store_dword v[28:29], v18, off offset:128
	ds_write_b128 v154, v[14:17]
	ds_write_b128 v153, v[10:13]
	ds_read_b128 v[10:13], v152
	ds_read_b128 v[14:17], v152 offset:1024
	v_mov_b32_e32 v22, 0
	v_add_co_u32_e32 v20, vcc, s68, v148
	s_waitcnt vmcnt(11) lgkmcnt(1)
	v_pk_add_f32 v[10:11], v[46:47], v[10:11]
	v_pk_add_f32 v[12:13], v[48:49], v[12:13]
	v_cvt_pk_fp8_f32 v22, v10, v11
	v_addc_co_u32_e32 v21, vcc, 0, v149, vcc
	global_store_dwordx4 v[20:21], v[10:13], off
	v_add_co_u32_e32 v20, vcc, s69, v148
	v_cvt_pk_fp8_f32 v22, v12, v13 op_sel:[0,0,1]
	s_mov_b64 s[10:11], 0x58000
	v_addc_co_u32_e32 v21, vcc, 0, v149, vcc
	v_lshl_add_u64 v[10:11], v[146:147], 0, s[10:11]
	s_mov_b32 s10, 0x58000
	v_add_co_u32_e32 v12, vcc, s10, v146
	s_waitcnt vmcnt(10) lgkmcnt(0)
	v_pk_add_f32 v[16:17], v[44:45], v[16:17]
	v_pk_add_f32 v[14:15], v[42:43], v[14:15]
	v_addc_co_u32_e32 v13, vcc, 0, v147, vcc
	global_store_dwordx4 v[20:21], v[14:17], off
	global_store_dword v[12:13], v22, off
	v_mov_b32_e32 v22, 0
	v_cvt_pk_fp8_f32 v22, v14, v15
	s_mov_b32 s10, 0x5c000
	v_add_co_u32_e32 v12, vcc, s10, v146
	v_cvt_pk_fp8_f32 v22, v16, v17 op_sel:[0,0,1]
	s_nop 0
	v_addc_co_u32_e32 v13, vcc, 0, v147, vcc
	v_lshl_add_u64 v[18:19], v[148:149], 0, s[28:29]
	global_store_dword v[12:13], v22, off
	ds_write_b128 v154, v[6:9]
	ds_write_b128 v153, v[2:5]
	ds_read_b128 v[2:5], v152
	ds_read_b128 v[6:9], v152 offset:1024
	v_mov_b32_e32 v14, 0
	v_readlane_b32 s82, v244, 0
	s_and_b64 vcc, exec, s[0:1]
	s_waitcnt lgkmcnt(1)
	v_pk_add_f32 v[4:5], v[40:41], v[4:5]
	v_pk_add_f32 v[2:3], v[38:39], v[2:3]
	s_waitcnt vmcnt(12) lgkmcnt(0)
	v_pk_add_f32 v[8:9], v[36:37], v[8:9]
	v_pk_add_f32 v[6:7], v[34:35], v[6:7]
	global_store_dwordx4 v[18:19], v[2:5], off offset:512
	global_store_dwordx4 v[20:21], v[6:9], off offset:512
	v_cvt_pk_fp8_f32 v14, v2, v3
	v_mov_b32_e32 v2, 0
	v_cvt_pk_fp8_f32 v2, v6, v7
	s_mov_b32 s74, s31
	v_cvt_pk_fp8_f32 v14, v4, v5 op_sel:[0,0,1]
	s_mov_b32 s33, s30
	v_cvt_pk_fp8_f32 v2, v8, v9 op_sel:[0,0,1]
	s_mov_b32 s78, s71
	s_mov_b32 s77, s70
	v_readlane_b32 s83, v244, 1
	s_mov_b32 s94, s55
	global_store_dword v[10:11], v14, off offset:128
	global_store_dword v[12:13], v2, off offset:128
	s_cbranch_vccz .LBB0_701
	s_waitcnt vmcnt(0)
	s_cmpk_gt_u32 s34, 0xff
	s_cbranch_scc1 .LBB0_712
	s_barrier
